# attention inner loop: mid-iteration wait/barrier selector reduced to a scalar compare chain with nothing after the barrier; has-next flag inversion and 0/1 value computed on the SALU instead of a VALU
# speedup vs baseline: 1.0058x; 1.0058x over previous
.LBB0_1324:
	v_mfma_f32_32x32x16_bf16 v[2:17], v[138:141], v[142:145], v[2:17]
	v_exp_f32_e32 v82, v82
	v_exp_f32_e32 v83, v83
	v_exp_f32_e32 v84, v84
	v_exp_f32_e32 v85, v85
	v_mfma_f32_32x32x16_bf16 v[18:33], v[138:141], v[146:149], v[18:33]
	v_exp_f32_e32 v86, v86
	v_exp_f32_e32 v87, v87
	v_exp_f32_e32 v88, v88
	v_exp_f32_e32 v89, v89
	s_and_b32 s54, s44, 3
	s_mulk_i32 s54, 0x2800
	v_add_u32_e32 v197, s54, v238
	ds_read_b128 v[138:141], v197
	ds_read_b128 v[130:133], v197 offset:512
	v_mfma_f32_32x32x16_bf16 v[2:17], v[50:53], v[54:57], v[2:17]
	v_exp_f32_e32 v90, v90
	v_exp_f32_e32 v91, v91
	v_exp_f32_e32 v92, v92
	v_exp_f32_e32 v93, v93
	ds_read_b128 v[134:137], v197 offset:2048
	ds_read_b128 v[126:129], v197 offset:2560
	v_mfma_f32_32x32x16_bf16 v[18:33], v[50:53], v[58:61], v[18:33]
	v_exp_f32_e32 v94, v94
	v_exp_f32_e32 v95, v95
	v_exp_f32_e32 v96, v96
	v_exp_f32_e32 v97, v97
	ds_read_b128 v[122:125], v197 offset:4096
	ds_read_b128 v[118:121], v197 offset:4608
	s_waitcnt lgkmcnt(12)
	v_mfma_f32_32x32x16_bf16 v[2:17], v[34:37], v[62:65], v[2:17]
	v_exp_f32_e32 v66, v66
	v_exp_f32_e32 v67, v67
	v_exp_f32_e32 v68, v68
	v_exp_f32_e32 v69, v69
	s_waitcnt lgkmcnt(10)
	v_mfma_f32_32x32x16_bf16 v[18:33], v[34:37], v[150:153], v[18:33]
	v_exp_f32_e32 v70, v70
	v_exp_f32_e32 v71, v71
	v_exp_f32_e32 v72, v72
	v_exp_f32_e32 v73, v73
	s_waitcnt lgkmcnt(8)
	v_mfma_f32_32x32x16_bf16 v[2:17], v[38:41], v[154:157], v[2:17]
	v_exp_f32_e32 v74, v74
	v_exp_f32_e32 v75, v75
	v_exp_f32_e32 v76, v76
	v_exp_f32_e32 v77, v77
	s_waitcnt lgkmcnt(6)
	v_mfma_f32_32x32x16_bf16 v[18:33], v[38:41], v[42:45], v[18:33]
	v_exp_f32_e32 v78, v78
	v_exp_f32_e32 v79, v79
	v_exp_f32_e32 v80, v80
	v_exp_f32_e32 v81, v81
	s_and_b64 s[52:53], s[52:53], exec
	s_cselect_b32 s54, s60, 1
	s_cmp_gt_i32 s54, 2
	s_cbranch_scc1 .Lattn_w3a
	s_cmp_eq_u32 s54, 2
	s_cbranch_scc1 .Lattn_w2a
	s_waitcnt vmcnt(1) lgkmcnt(0)
	s_barrier
	s_branch .LBB0_1331
.Lattn_w2a:
	s_waitcnt vmcnt(2) lgkmcnt(0)
	s_barrier
	s_branch .LBB0_1331
.Lattn_w3a:
	s_waitcnt vmcnt(3) lgkmcnt(0)
	s_barrier

.LBB0_1338:
	v_mfma_f32_32x32x16_bf16 v[2:17], v[154:157], v[162:165], v[2:17]
	v_exp_f32_e32 v50, v50
	v_exp_f32_e32 v51, v51
	v_exp_f32_e32 v52, v52
	v_exp_f32_e32 v53, v53
	v_mfma_f32_32x32x16_bf16 v[18:33], v[154:157], v[158:161], v[18:33]
	v_exp_f32_e32 v54, v54
	v_exp_f32_e32 v55, v55
	v_exp_f32_e32 v56, v56
	v_exp_f32_e32 v57, v57
	s_not_b64 s[44:45], s[58:59]
	s_and_b32 s101, s58, 1
	s_andn2_b64 vcc, exec, s[58:59]
	s_cbranch_vccnz .LBB0_1340
	s_and_b32 s55, s54, 3
	s_mulk_i32 s55, 0x2800
	v_add_u32_e32 v79, s55, v238
	ds_read_b128 v[138:141], v79
	ds_read_b128 v[130:133], v79 offset:512

.LBB0_1344:
	s_waitcnt lgkmcnt(6)
	v_mfma_f32_32x32x16_bf16 v[2:17], v[82:85], v[90:93], v[2:17]
	v_exp_f32_e32 v34, v34
	v_exp_f32_e32 v35, v35
	v_exp_f32_e32 v36, v36
	v_exp_f32_e32 v37, v37
	s_waitcnt lgkmcnt(4)
	v_mfma_f32_32x32x16_bf16 v[18:33], v[82:85], v[86:89], v[18:33]
	v_exp_f32_e32 v38, v38
	v_exp_f32_e32 v39, v39
	v_exp_f32_e32 v40, v40
	v_exp_f32_e32 v41, v41
	s_waitcnt lgkmcnt(2)
	v_mfma_f32_32x32x16_bf16 v[2:17], v[66:69], v[70:73], v[2:17]
	v_exp_f32_e32 v42, v42
	v_exp_f32_e32 v43, v43
	v_exp_f32_e32 v44, v44
	v_exp_f32_e32 v45, v45
	s_waitcnt lgkmcnt(0)
	v_mfma_f32_32x32x16_bf16 v[18:33], v[66:69], v[74:77], v[18:33]
	v_exp_f32_e32 v46, v46
	v_exp_f32_e32 v47, v47
	v_exp_f32_e32 v48, v48
	v_exp_f32_e32 v49, v49
	s_and_b64 s[44:45], s[52:53], exec
	s_cselect_b32 s58, s69, 0
	s_mov_b32 s44, s101
	s_add_i32 s58, s58, s44
	s_mov_b64 s[54:55], -1
	s_mov_b64 s[44:45], 0
	s_cmp_lt_i32 s58, 2
	s_mov_b64 s[52:53], 0
	s_cbranch_scc0 .LBB0_1351
	s_and_b64 vcc, exec, s[54:55]
	s_cbranch_vccnz .LBB0_1358
